# band attention epilogue: the two cross-half exchanges (softmax denominator, sum of squares) use v_permlane32_swap instead of ds_bpermute
# baseline (speedup 1.0000x reference)
; __device__ __forceinline__ void unit(LAS unsigned char* lds, const bf16* __restrict__ Q, const bf16* __restrict__ Kp, const bf16* __restrict__ VT, const float* __restrict__ rel, bf16* mix, float* ssa, int b, int h, int u) {
;     ...
;     const float lden = hh == 0 ? o2[0] : 0.f;
;     const float inv = 1.0f / (lden + __shfl_xor(lden, 32)); float ss = 0.f;
; #pragma unroll
;     for (int r = 0; r < 16; ++r) { o0[r] *= inv; o1[r] *= inv; ss += o0[r] * o0[r] + o1[r] * o1[r]; }
;     ss += __shfl_xor(ss, 32); if (hh == 0) ssa[tok * 16 + h] = ss;
.LBB5_1001:
	v_cndmask_b32_e64 v2, 0, v50, s[4:5]
	v_mov_b32_e32 v4, v2
	s_nop 1
	v_permlane32_swap_b32 v4, v2
	s_waitcnt lgkmcnt(0)
	v_add_f32_e32 v2, v2, v4
	v_div_scale_f32 v4, s[38:39], v2, v2, 1.0
	v_rcp_f32_e32 v5, v4
	v_div_scale_f32 v6, vcc, 1.0, v2, 1.0
	v_fma_f32 v7, -v4, v5, 1.0
	v_fmac_f32_e32 v5, v7, v5
	v_mul_f32_e32 v7, v6, v5
	v_fma_f32 v8, -v4, v7, v6
	v_fmac_f32_e32 v7, v8, v5
	v_fma_f32 v4, -v4, v7, v6
	v_div_fmas_f32 v4, v4, v5, v7
	v_div_fixup_f32 v51, v4, v2, 1.0
	v_mul_f32_e32 v2, v34, v51
	v_mul_f32_e32 v4, v35, v51
	v_mul_f32_e32 v6, v18, v51
	v_mul_f32_e32 v5, v2, v2
	v_mul_f32_e32 v10, v19, v51
	v_mul_f32_e32 v7, v4, v4
	v_fmac_f32_e32 v5, v6, v6
	v_fmac_f32_e32 v7, v10, v10
	v_add_f32_e32 v5, v5, v7
	v_mul_f32_e32 v7, v36, v51
	v_mul_f32_e32 v14, v20, v51
	v_mul_f32_e32 v8, v7, v7
	v_fmac_f32_e32 v8, v14, v14
	v_mul_f32_e32 v12, v37, v51
	v_add_f32_e32 v5, v8, v5
	v_mul_f32_e32 v21, v21, v51
	v_mul_f32_e32 v8, v12, v12
	v_fmac_f32_e32 v8, v21, v21
	v_add_f32_e32 v8, v8, v5
	v_mul_f32_e32 v5, v38, v51
	v_mul_f32_e32 v11, v22, v51
	v_mul_f32_e32 v9, v5, v5
	v_fmac_f32_e32 v9, v11, v11
	v_add_f32_e32 v9, v9, v8
	v_mul_f32_e32 v8, v39, v51
	v_mul_f32_e32 v17, v23, v51
	v_mul_f32_e32 v13, v8, v8
	v_fmac_f32_e32 v13, v17, v17
	v_add_f32_e32 v9, v13, v9
	v_mul_f32_e32 v13, v40, v51
	v_mul_f32_e32 v22, v24, v51
	v_mul_f32_e32 v15, v13, v13
	v_fmac_f32_e32 v15, v22, v22
	v_mul_f32_e32 v19, v41, v51
	v_add_f32_e32 v9, v15, v9
	v_mul_f32_e32 v34, v25, v51
	v_mul_f32_e32 v15, v19, v19
	v_fmac_f32_e32 v15, v34, v34
	v_add_f32_e32 v15, v15, v9
	v_mul_f32_e32 v9, v42, v51
	v_mul_f32_e32 v18, v26, v51
	v_mul_f32_e32 v16, v9, v9
	v_fmac_f32_e32 v16, v18, v18
	v_add_f32_e32 v16, v16, v15
	v_mul_f32_e32 v15, v43, v51
	v_mul_f32_e32 v24, v27, v51
	v_mul_f32_e32 v20, v15, v15
	v_fmac_f32_e32 v20, v24, v24
	v_add_f32_e32 v16, v20, v16
	v_mul_f32_e32 v20, v44, v51
	v_mul_f32_e32 v28, v28, v51
	v_mul_f32_e32 v23, v20, v20
	v_fmac_f32_e32 v23, v28, v28
	v_mul_f32_e32 v26, v45, v51
	v_add_f32_e32 v16, v23, v16
	v_mul_f32_e32 v35, v29, v51
	v_mul_f32_e32 v23, v26, v26
	v_fmac_f32_e32 v23, v35, v35
	v_add_f32_e32 v23, v23, v16
	v_mul_f32_e32 v16, v46, v51
	v_mul_f32_e32 v25, v30, v51
	v_mul_f32_e32 v27, v16, v16
	v_fmac_f32_e32 v27, v25, v25
	v_add_f32_e32 v27, v27, v23
	v_mul_f32_e32 v23, v47, v51
	v_mul_f32_e32 v29, v31, v51
	v_mul_f32_e32 v30, v23, v23
	v_fmac_f32_e32 v30, v29, v29
	v_add_f32_e32 v30, v30, v27
	v_mul_f32_e32 v27, v48, v51
	v_mul_f32_e32 v31, v32, v51
	v_mul_f32_e32 v32, v27, v27
	v_fmac_f32_e32 v32, v31, v31
	v_add_f32_e32 v36, v32, v30
	v_mul_f32_e32 v30, v49, v51
	v_mul_f32_e32 v32, v33, v51
	v_mul_f32_e32 v33, v30, v30
	v_fmac_f32_e32 v33, v32, v32
	v_add_f32_e32 v33, v33, v36
	v_mov_b32_e32 v36, v33
	s_nop 1
	v_permlane32_swap_b32 v36, v33
	s_and_saveexec_b64 s[38:39], s[4:5]
	s_cbranch_execz .LBB5_978
	s_waitcnt lgkmcnt(0)
	v_add_f32_e32 v33, v33, v36
	v_lshlrev_b64 v[36:37], 6, v[164:165]
	v_lshl_add_u64 v[36:37], s[34:35], 0, v[36:37]
	s_lshl_b32 s36, s29, 2
	v_lshl_add_u64 v[36:37], v[36:37], 0, s[36:37]
	global_store_dword v[36:37], v33, off
	s_branch .LBB5_978
